# baseline (speedup 1.0000x reference)
_Z6gemm_kILi1ELb1ELb1ELb0ELb0ELb1EEvPKtS1_ii7EpiArgs:
	s_load_dwordx8 s[4:11], s[0:1], 0x0
	s_load_dwordx2 s[14:15], s[0:1], 0x30
	s_load_dwordx2 s[12:13], s[0:1], 0x48
	s_lshl_b32 s0, s2, 3
	s_and_b32 s0, s0, 56
	s_bfe_u32 s1, s2, 0x30003
	s_or_b32 s0, s0, s1
	s_lshl_b32 s22, s0, 7
	v_readfirstlane_b32 s18, v0
	s_lshr_b32 s1, s2, 6
	s_waitcnt lgkmcnt(0)
	s_mul_hi_i32 s3, s9, s22
	s_mul_i32 s2, s9, s22
	s_lshr_b32 s19, s18, 6
	s_bfe_u32 s23, s18, 0x20006
	s_ashr_i32 s17, s9, 31
	s_lshl_b64 s[2:3], s[2:3], 1
	s_mul_i32 s0, s1, 0xc0
	s_add_u32 s2, s4, s2
	s_addc_u32 s3, s5, s3
	s_mul_hi_i32 s5, s9, s0
	s_mul_i32 s4, s9, s0
	s_ashr_i32 s1, s0, 31
	s_lshl_b64 s[4:5], s[4:5], 1
	s_add_u32 s4, s6, s4
	v_lshrrev_b32_e32 v1, 4, v0
	s_addc_u32 s5, s7, s5
	s_lshr_b32 s6, s18, 2
	v_xor_b32_e32 v4, v1, v0
	s_lshl_b32 s25, s19, 10
	s_and_b32 s6, s6, 0x3fffffc0
	v_and_b32_e32 v2, 15, v0
	v_lshrrev_b32_e32 v3, 3, v0
	v_lshlrev_b32_e32 v4, 3, v4
	v_bfe_u32 v5, v0, 1, 3
	s_cmp_lg_u32 0, -1
	v_mul_lo_u32 v3, s9, v3
	v_and_b32_e32 v4, 56, v4
	s_mov_b32 s16, s9
	v_bitop3_b32 v5, v1, v5, 3 bitop3:0x6c
	v_or_b32_e32 v1, s6, v2
	s_cselect_b32 s6, 0, 0
	v_add_lshl_u32 v84, v3, v4, 1
	s_add_i32 s25, s25, s6
	s_nop 4
	s_mov_b32 s6, m0
	s_mov_b32 m0, s25
	s_nop 0
	global_load_lds_dwordx4 v84, s[2:3]
	s_mov_b32 m0, s6
	s_lshl_b64 s[18:19], s[16:17], 7
	s_add_u32 s6, s2, s18
	s_addc_u32 s7, s3, s19
	s_add_i32 s26, s25, 0x2000
	s_nop 4
	s_mov_b32 s16, m0
	s_mov_b32 m0, s26
	s_nop 0
	global_load_lds_dwordx4 v84, s[6:7]
	s_mov_b32 m0, s16
	s_add_i32 s27, s25, 0x4000
	s_nop 4
	s_mov_b32 s16, m0
	s_mov_b32 m0, s27
	s_nop 0
	global_load_lds_dwordx4 v84, s[4:5]
	s_mov_b32 m0, s16
	s_add_u32 s16, s4, s18
	s_addc_u32 s17, s5, s19
	s_add_i32 s28, s25, 0x6000
	s_nop 4
	s_mov_b32 s20, m0
	s_mov_b32 m0, s28
	s_nop 0
	global_load_lds_dwordx4 v84, s[16:17]
	s_mov_b32 m0, s20
	s_add_u32 s18, s16, s18
	s_addc_u32 s19, s17, s19
	s_add_i32 s29, s25, 0x8000
	s_nop 4
	s_mov_b32 s20, m0
	s_mov_b32 m0, s29
	s_nop 0
	global_load_lds_dwordx4 v84, s[18:19]
	s_mov_b32 m0, s20
	s_add_u32 s20, s2, 0x80
	s_addc_u32 s21, s3, 0
	s_add_i32 s30, s25, 0xa000
	s_nop 4
	s_mov_b32 s31, m0
	s_mov_b32 m0, s30
	s_nop 0
	global_load_lds_dwordx4 v84, s[20:21]
	s_mov_b32 m0, s31
	s_add_u32 s20, s6, 0x80
	s_addc_u32 s21, s7, 0
	s_add_i32 s31, s25, 0xc000
	s_nop 4
	s_mov_b32 s33, m0
	s_mov_b32 m0, s31
	s_nop 0
	global_load_lds_dwordx4 v84, s[20:21]
	s_mov_b32 m0, s33
	s_add_u32 s20, s4, 0x80
	s_addc_u32 s21, s5, 0
	s_add_i32 s33, s25, 0xe000
	s_nop 4
	s_mov_b32 s34, m0
	s_mov_b32 m0, s33
	s_nop 0
	global_load_lds_dwordx4 v84, s[20:21]
	s_mov_b32 m0, s34
	s_add_u32 s20, s16, 0x80
	s_addc_u32 s21, s17, 0
	s_add_i32 s34, s25, 0x10000
	s_nop 4
	s_mov_b32 s35, m0
	s_mov_b32 m0, s34
	s_nop 0
	global_load_lds_dwordx4 v84, s[20:21]
	s_mov_b32 m0, s35
	s_add_u32 s20, s18, 0x80
	s_addc_u32 s21, s19, 0
	s_add_i32 s35, s25, 0x12000
	s_nop 4
	s_mov_b32 s36, m0
	s_mov_b32 m0, s35
	s_nop 0
	global_load_lds_dwordx4 v84, s[20:21]
	s_mov_b32 m0, s36
	s_add_u32 s20, s2, 0x100
	s_addc_u32 s21, s3, 0
	s_add_i32 s36, s25, 0x14000
	s_nop 4
	s_mov_b32 s37, m0
	s_mov_b32 m0, s36
	s_nop 0
	global_load_lds_dwordx4 v84, s[20:21]
	s_mov_b32 m0, s37
	s_add_u32 s20, s6, 0x100
	s_addc_u32 s21, s7, 0
	s_add_i32 s37, s25, 0x16000
	s_nop 4
	s_mov_b32 s38, m0
	s_mov_b32 m0, s37
	s_nop 0
	global_load_lds_dwordx4 v84, s[20:21]
	s_mov_b32 m0, s38
	s_add_u32 s20, s4, 0x100
	s_addc_u32 s21, s5, 0
	s_add_i32 s38, s25, 0x18000
	s_nop 4
	s_mov_b32 s39, m0
	s_mov_b32 m0, s38
	s_nop 0
	global_load_lds_dwordx4 v84, s[20:21]
	s_mov_b32 m0, s39
	s_add_u32 s20, s16, 0x100
	s_addc_u32 s21, s17, 0
	s_add_i32 s39, s25, 0x1a000
	s_mul_i32 s23, s23, 48
	s_nop 4
	s_mov_b32 s40, m0
	s_mov_b32 m0, s39
	s_nop 0
	global_load_lds_dwordx4 v84, s[20:21]
	s_mov_b32 m0, s40
	s_add_u32 s20, s18, 0x100
	v_lshlrev_b32_e32 v5, 4, v5
	v_or_b32_e32 v2, s23, v2
	v_lshl_add_u32 v31, v1, 7, 0
	s_addc_u32 s21, s19, 0
	s_add_i32 s40, s25, 0x1c000
	s_nop 4
	s_mov_b32 s41, m0
	s_mov_b32 m0, s40
	s_nop 0
	global_load_lds_dwordx4 v84, s[20:21]
	s_mov_b32 m0, s41
	v_xor_b32_e32 v30, 64, v5
	v_lshl_add_u32 v2, v2, 7, 0
	v_add_u32_e32 v79, v31, v5
	s_waitcnt vmcnt(10) lgkmcnt(0)
	s_barrier
	v_add_u32_e32 v82, v2, v5
	v_add_u32_e32 v81, v2, v30
	s_ashr_i32 s9, s9, 6
	v_add_u32_e32 v83, v31, v30
	s_mul_i32 s70, s22, s8
	s_add_u32 s70, s70, s0
	s_lshl_b32 s71, s70, 1
	s_add_u32 s72, s12, s71
	s_addc_u32 s73, s13, 0
	s_lshl_b32 s71, s70, 2
	s_add_u32 s74, s10, s71
	s_addc_u32 s75, s11, 0
	s_movk_i32 s76, 0xffd0
	v_add_u32_e32 v100, 0x14000, v79
	v_add_u32_e32 v101, 0x14000, v83
	v_add_u32_e32 v102, 0x14000, v82
	v_add_u32_e32 v103, 0x14000, v81
	s_add_u32 s54, s2, 0x100
	s_addc_u32 s55, s3, 0
	s_add_u32 s56, s6, 0x100
	s_addc_u32 s57, s7, 0
	s_add_u32 s58, s4, 0x100
	s_addc_u32 s59, s5, 0
	s_add_u32 s60, s16, 0x100
	s_addc_u32 s61, s17, 0
	s_add_u32 s62, s18, 0x100
	s_addc_u32 s63, s19, 0
	s_mul_hi_u32 s64, s9, 0x55555556
	s_add_i32 s64, s64, -1
	ds_read_b128 v[168:171], v79 offset:0
	ds_read_b128 v[184:187], v82 offset:16384
	ds_read_b128 v[188:191], v82 offset:18432
	ds_read_b128 v[192:195], v82 offset:20480
	ds_read_b128 v[172:175], v79 offset:2048
	ds_read_b128 v[176:179], v79 offset:4096
	ds_read_b128 v[180:183], v79 offset:6144
	v_mov_b32_e32 v120, 0
	v_mov_b32_e32 v121, 0
	v_mov_b32_e32 v122, 0
	v_mov_b32_e32 v123, 0
	v_mov_b32_e32 v124, 0
	v_mov_b32_e32 v125, 0
	v_mov_b32_e32 v126, 0
	v_mov_b32_e32 v127, 0
	v_mov_b32_e32 v128, 0
	v_mov_b32_e32 v129, 0
	v_mov_b32_e32 v130, 0
	v_mov_b32_e32 v131, 0
	v_mov_b32_e32 v132, 0
	v_mov_b32_e32 v133, 0
	v_mov_b32_e32 v134, 0
	v_mov_b32_e32 v135, 0
	v_mov_b32_e32 v136, 0
	v_mov_b32_e32 v137, 0
	v_mov_b32_e32 v138, 0
	v_mov_b32_e32 v139, 0
	v_mov_b32_e32 v140, 0
	v_mov_b32_e32 v141, 0
	v_mov_b32_e32 v142, 0
	v_mov_b32_e32 v143, 0
	v_mov_b32_e32 v144, 0
	v_mov_b32_e32 v145, 0
	v_mov_b32_e32 v146, 0
	v_mov_b32_e32 v147, 0
	v_mov_b32_e32 v148, 0
	v_mov_b32_e32 v149, 0
	v_mov_b32_e32 v150, 0
	v_mov_b32_e32 v151, 0
	v_mov_b32_e32 v152, 0
	v_mov_b32_e32 v153, 0
	v_mov_b32_e32 v154, 0
	v_mov_b32_e32 v155, 0
	v_mov_b32_e32 v156, 0
	v_mov_b32_e32 v157, 0
	v_mov_b32_e32 v158, 0
	v_mov_b32_e32 v159, 0
	v_mov_b32_e32 v160, 0
	v_mov_b32_e32 v161, 0
	v_mov_b32_e32 v162, 0
	v_mov_b32_e32 v163, 0
	v_mov_b32_e32 v164, 0
	v_mov_b32_e32 v165, 0
	v_mov_b32_e32 v166, 0
	v_mov_b32_e32 v167, 0
	s_waitcnt lgkmcnt(0)
	v_mfma_f32_16x16x32_f16 v[120:123], v[184:187], v[168:171], v[120:123]
	ds_read_b128 v[196:199], v83 offset:0
	v_mfma_f32_16x16x32_f16 v[124:127], v[188:191], v[168:171], v[124:127]
	ds_read_b128 v[212:215], v81 offset:16384
	v_mfma_f32_16x16x32_f16 v[128:131], v[192:195], v[168:171], v[128:131]
	ds_read_b128 v[216:219], v81 offset:18432
	v_mfma_f32_16x16x32_f16 v[132:135], v[184:187], v[172:175], v[132:135]
	ds_read_b128 v[220:223], v81 offset:20480
	v_mfma_f32_16x16x32_f16 v[136:139], v[188:191], v[172:175], v[136:139]
	ds_read_b128 v[200:203], v83 offset:2048
	v_mfma_f32_16x16x32_f16 v[140:143], v[192:195], v[172:175], v[140:143]
	ds_read_b128 v[204:207], v83 offset:4096
	v_mfma_f32_16x16x32_f16 v[144:147], v[184:187], v[176:179], v[144:147]
	ds_read_b128 v[208:211], v83 offset:6144
	v_mfma_f32_16x16x32_f16 v[148:151], v[188:191], v[176:179], v[148:151]
	v_mfma_f32_16x16x32_f16 v[152:155], v[192:195], v[176:179], v[152:155]
	v_mfma_f32_16x16x32_f16 v[156:159], v[184:187], v[180:183], v[156:159]
	v_mfma_f32_16x16x32_f16 v[160:163], v[188:191], v[180:183], v[160:163]
	v_mfma_f32_16x16x32_f16 v[164:167], v[192:195], v[180:183], v[164:167]
	s_cmp_ge_u32 s25, 0x1000
	s_cbranch_scc1 .Lgk_loop_dnB
